# baseline (speedup 1.0000x reference)
.Lk2_epi:
	s_waitcnt vmcnt(0) lgkmcnt(0)
	s_nop 15
	v_lshlrev_b32_e32 v175, 6, v172
	v_lshl_or_b32 v175, v173, 4, v175
	v_cvt_pk_f16_f32 v184, v16, v17
	v_cvt_pk_f16_f32 v185, v18, v19
	v_cvt_pk_f16_f32 v186, v20, v21
	v_cvt_pk_f16_f32 v187, v22, v23
	v_cvt_pk_f16_f32 v188, v24, v25
	v_cvt_pk_f16_f32 v189, v26, v27
	v_cvt_pk_f16_f32 v190, v28, v29
	v_cvt_pk_f16_f32 v191, v30, v31
	v_cvt_pk_f16_f32 v176, v0, v1
	v_cvt_pk_f16_f32 v177, v2, v3
	v_cvt_pk_f16_f32 v178, v4, v5
	v_cvt_pk_f16_f32 v179, v6, v7
	v_cvt_pk_f16_f32 v180, v8, v9
	v_cvt_pk_f16_f32 v181, v10, v11
	v_cvt_pk_f16_f32 v182, v12, v13
	v_cvt_pk_f16_f32 v183, v14, v15
	s_lshl_b32 s36, s10, 18
	s_add_u32 s0, s6, s36
	s_addc_u32 s1, s7, 0
	s_lshl_b32 s36, s11, 3
	s_add_u32 s36, s36, s33
	s_lshl_b32 s36, s36, 12
	s_add_u32 s0, s0, s36
	s_addc_u32 s1, s1, 0
	v_permlane32_swap_b32 v184, v186
	v_permlane32_swap_b32 v185, v187
	v_permlane32_swap_b32 v188, v190
	v_permlane32_swap_b32 v189, v191
	v_permlane32_swap_b32 v176, v178
	v_permlane32_swap_b32 v177, v179
	v_permlane32_swap_b32 v180, v182
	v_permlane32_swap_b32 v181, v183
	global_store_dwordx4 v175, v[184:187], s[0:1] sc0 sc1
	global_store_dwordx4 v175, v[188:191], s[0:1] offset:32 sc0 sc1
	global_store_dwordx4 v175, v[176:179], s[0:1] offset:2048 sc0 sc1
	global_store_dwordx4 v175, v[180:183], s[0:1] offset:2080 sc0 sc1
	s_endpgm
